# router weights stored in MFMA fragment order (contiguous 1 KiB B-fragment loads in the router; producer iterates the new layout)
# speedup vs baseline: 1.0072x; 1.0072x over previous
; __device__ __forceinline__ unsigned f2bf(float f) { unsigned u = __builtin_bit_cast(unsigned, f); return (u + 0x7fffu + ((u >> 16) & 1u)) >> 16; }
; __device__ __forceinline__ void late_prep(const Args& a, unsigned char* lds_g, int gw, int NGW, int lane, int wave) {
;     ...
;         for (int idx = gw * 64 + lane; idx < 4 * 48 * 2048; idx += NGW * 64) { const int k = idx & 2047, j = (idx >> 11) % 48, b = idx / (48 * 2048);
;             const float gm = a.in[I_N2G][k] * (1.f + MODr[b * 12288 + 4 * 2048 + k]);
;             const float wv = j < 32 ? a.in[I_WRE][(size_t)k * 32 + j] : (j < 36 ? a.in[I_WRG][(size_t)k * 4 + (j - 32)] : 0.f);
;             const float v_ = gm * wv; const unsigned hi_ = f2bf(v_); WRh[idx] = (bf16)hi_; WRl[idx] = (bf16)f2bf(v_ - bf2f(hi_)); }
.LBB0_195:
	v_bfe_u32 v68, v0, 3, 4
	v_bfe_u32 v69, v0, 7, 8
	v_and_b32_e32 v70, 0xffff8007, v0
	v_lshl_or_b32 v70, v68, 11, v70
	v_lshl_or_b32 v68, v69, 3, v70
	v_mul_hi_i32 v1, v0, s3
	v_lshrrev_b32_e32 v6, 31, v1
	v_ashrrev_i32_e32 v1, 14, v1
	v_add_u32_e32 v6, v1, v6
	v_and_b32_e32 v4, 0x7ff, v68
	s_load_dwordx16 s[36:51], s[96:97], 0x80
	v_mul_i32_i24_e32 v6, 0x3000, v6
	v_or_b32_e32 v6, v6, v4
	v_add_u32_e32 v6, 0x2000, v6
	v_ashrrev_i32_e32 v7, 31, v6
	v_lshlrev_b32_e32 v1, 2, v4
	v_lshl_add_u64 v[6:7], v[6:7], 2, s[12:13]
	s_waitcnt lgkmcnt(0)
	global_load_dword v1, v1, s[44:45]
	s_nop 0
	global_load_dword v8, v[6:7], off
	v_ashrrev_i32_e32 v6, 11, v68
	v_mul_hi_i32 v7, v6, s3
	v_lshrrev_b32_e32 v9, 31, v7
	v_lshrrev_b32_e32 v7, 3, v7
	v_add_u32_e32 v7, v7, v9
	v_mul_lo_u32 v7, v7, 48
	v_sub_u32_e32 v6, v6, v7
	v_cmp_lt_i32_e32 vcc, 31, v6
	s_and_saveexec_b64 s[0:1], vcc
	s_xor_b64 s[18:19], exec, s[0:1]
	s_cbranch_execz .LBB0_199
	v_cmp_gt_u32_e32 vcc, 36, v6
	v_mov_b32_e32 v7, 0
	s_and_saveexec_b64 s[0:1], vcc
	s_cbranch_execz .LBB0_198
	s_load_dwordx16 s[36:51], s[96:97], 0x80
	v_lshlrev_b32_e32 v4, 4, v4
	v_mov_b32_e32 v7, v5
	s_waitcnt lgkmcnt(0)
	v_lshl_add_u64 v[10:11], s[46:47], 0, v[4:5]
	v_lshl_add_u64 v[6:7], v[6:7], 2, v[10:11]
	global_load_dword v7, v[6:7], off offset:-128

; __device__ __forceinline__ void phase_router(const Args& a, unsigned char* lds_g, int tid, int lane, int wave) {
;     ...
;     const int slot = wave >> 2, kq = wave & 3, i = lane & 15, gq = lane >> 4;
;     const bool shp = gridDim.x == 256; f32x4* PSH = (f32x4*)(lds_g + 65536);
;     if (shp) { const int t_ = wave * 64 + lane, c_ = 4 * t_, b_ = (32 * (int)blockIdx.x) >> 11;
;         const f32x4 gg = *(const f32x4*)(g + c_), sc = *(const f32x4*)(MOD + b_ * 12288 + 4 * 2048 + c_); PSH[t_] = gg * (sc + 1.f); PSH[512 + t_] = *(const f32x4*)(MOD + b_ * 12288 + 3 * 2048 + c_); }
;     for (int tp = blockIdx.x; tp < NLAT / 32; tp += gridDim.x) {
;         const int tok0 = 32 * tp + 16 * slot, b = tok0 >> 11, kbase = wave * 256 + 8 * gq;
;         const bf16* xr0 = X1 + (size_t)(32 * tp + i) * D + kbase; const bf16* xr1 = xr0 + (size_t)16 * D;
;         const bf16* wh = WRh + ((size_t)(b * 48 + i) * 2048 + kbase); const bf16* wl = WRl + ((size_t)(b * 48 + i) * 2048 + kbase);
;         f32x4 ac[2][3]; float sq0 = 0.f, sq1 = 0.f;
.LBB0_972:
	s_cmpk_gt_i32 s83, 0xff
	s_cbranch_scc1 .LBB0_1113
	s_add_u32 s20, s84, 0x7c0000
	v_mbcnt_lo_u32_b32 v2, -1, 0
	s_addc_u32 s21, s85, 0
	v_mbcnt_hi_u32_b32 v2, -1, v2
	s_add_u32 s22, s84, 0x480000
	v_and_b32_e32 v5, 64, v2
	s_addc_u32 s23, s85, 0
	v_xor_b32_e32 v3, 16, v2
	v_add_u32_e32 v6, 64, v5
	s_mov_b64 s[6:7], src_shared_base
	s_add_u32 s24, s84, 0x380000
	v_cmp_lt_i32_e32 vcc, v3, v6
	s_addc_u32 s25, s85, 0
	s_lshr_b32 s6, s4, 6
	s_lshl_b32 s100, s6, 13
	v_cndmask_b32_e32 v3, v2, v3, vcc
	v_lshlrev_b32_e32 v62, 2, v60
	s_lshl_b32 s5, s6, 2
	v_lshlrev_b32_e32 v175, 2, v3
	v_xor_b32_e32 v3, 32, v2
	s_and_b32 s26, s4, 0xffffffc0
	v_lshrrev_b32_e32 v1, 4, v60
	v_add_u32_e32 v0, 0, v62
	s_and_b32 s36, s5, 0xffffff0
	v_cmp_lt_i32_e32 vcc, v3, v6
	s_lshl_b32 s28, s6, 4
	s_add_i32 s29, s26, 0
	v_and_b32_e32 v174, 15, v60
	v_cndmask_b32_e32 v2, v2, v3, vcc
	v_mad_u64_u32 v[64:65], s[0:1], v60, 12, v[0:1]
	s_cmpk_lt_u32 s4, 0x80
	s_mul_i32 s4, s6, 0x1c0
	v_lshlrev_b32_e32 v176, 2, v2
	v_add_u32_e32 v65, s26, v0
	v_add_u32_e32 v177, s29, v62
	s_cselect_b64 s[26:27], -1, 0
	s_add_i32 s29, s29, s4
	v_lshlrev_b32_e32 v0, 2, v174
	s_movk_i32 s30, 0xc0
	v_or_b32_e32 v2, 0xc0, v62
	v_add_u32_e32 v181, s28, v60
	v_add_u32_e32 v178, s29, v0
	v_add_u32_e32 v179, s29, v2
	v_or_b32_e32 v2, 0x1c0, v62
	v_add_u32_e32 v6, 0, v0
	v_mul_lo_u32 v0, v181, s30
	s_lshl_b32 s4, s36, 2
	v_mov_b32_e32 v61, 0
	v_lshlrev_b32_e32 v4, 3, v1
	v_add_u32_e32 v180, s29, v2
	v_lshlrev_b32_e32 v2, 2, v1
	v_add_u32_e32 v182, 0, v0
	s_and_b32 s37, s5, 12
	s_add_i32 s40, s4, 0
	v_lshl_add_u64 v[0:1], v[60:61], 3, s[84:85]
	s_mov_b64 s[4:5], 0x2ea00000
	v_lshl_add_u64 v[66:67], v[0:1], 0, s[4:5]
	v_lshl_add_u64 v[0:1], v[60:61], 2, s[84:85]
	s_mov_b64 s[4:5], 0x1c800000
	v_readlane_b32 s44, v249, 6
	v_or_b32_e32 v3, s28, v2
	v_lshl_add_u64 v[68:69], v[0:1], 0, s[4:5]
	s_add_i32 s4, 0, 0x10000
	v_or_b32_e32 v0, v5, v2
	v_readlane_b32 s45, v249, 7
	v_readlane_b32 s52, v249, 14
	v_readlane_b32 s53, v249, 15
	v_cmp_gt_u32_e64 s[0:1], 16, v60
	v_lshl_add_u32 v183, v60, 4, s4
	v_lshlrev_b32_e32 v184, 2, v0
	v_mul_lo_u32 v7, v3, s30
	s_lshl_b32 s4, s37, 2
	v_mov_b32_e32 v63, v61
	v_readlane_b32 s46, v249, 8
	v_readlane_b32 s47, v249, 9
	v_readlane_b32 s48, v249, 10
	v_readlane_b32 s49, v249, 11
	v_readlane_b32 s50, v249, 12
	v_readlane_b32 s51, v249, 13
	v_readlane_b32 s54, v249, 16
	v_readlane_b32 s55, v249, 17
	s_mov_b64 s[44:45], s[52:53]
	v_or_b32_e32 v60, 0x100, v62
	v_or_b32_e32 v0, 0x200, v62
	v_mov_b32_e32 v1, v61
	v_or_b32_e32 v2, 0x300, v62
	v_mov_b32_e32 v3, v61
	v_or_b32_e32 v80, 0x400, v62
	v_mov_b32_e32 v81, v61
	v_or_b32_e32 v86, 0x500, v62
	v_mov_b32_e32 v87, v61
	v_or_b32_e32 v92, 0x600, v62
	v_mov_b32_e32 v93, v61
	v_or_b32_e32 v98, 0x700, v62
	v_mov_b32_e32 v99, v61
	v_lshl_add_u32 v4, s6, 8, v4
	v_mov_b32_e32 v5, v61
	s_mul_i32 s38, s6, 0xc00
	s_mul_i32 s39, s6, 0x6000
	v_or_b32_e32 v185, 4, v184
	v_or_b32_e32 v186, 8, v184
	v_or_b32_e32 v187, 12, v184
	s_add_i32 s40, s40, s4
	v_lshl_add_u64 v[70:71], v[62:63], 2, s[44:45]
	v_add_u32_e32 v72, 0x2000, v183
	v_mov_b32_e32 v73, s7
	v_add_u32_e32 v74, 0x2400, v183
	v_mov_b32_e32 v75, s7
	v_add_u32_e32 v76, 0x2800, v183
	v_mov_b32_e32 v77, s7
	v_add_u32_e32 v78, 0x2c00, v183
	v_mov_b32_e32 v79, s7
	v_lshl_add_u64 v[82:83], v[80:81], 2, s[44:45]
	v_add_u32_e32 v84, 0x3000, v183
	v_mov_b32_e32 v85, s7
	v_lshl_add_u64 v[88:89], v[86:87], 2, s[44:45]
	v_add_u32_e32 v90, 0x3400, v183
	v_mov_b32_e32 v91, s7
	v_lshl_add_u64 v[94:95], v[92:93], 2, s[44:45]
	v_add_u32_e32 v96, 0x3800, v183
	v_mov_b32_e32 v97, s7
	v_lshl_add_u64 v[100:101], v[98:99], 2, s[44:45]
	v_add_u32_e32 v102, 0x3c00, v183
	v_mov_b32_e32 v103, s7
	s_or_b32 s41, s37, 1
	s_or_b32 s42, s37, 2
	s_or_b32 s43, s37, 3
	v_lshl_add_u64 v[104:105], v[4:5], 1, s[84:85]
	v_lshl_or_b32 v106, s83, 5, v174
	s_lshl_b32 s44, s82, 5
	s_mov_b32 s45, 0x2ea00000
	s_mov_b32 s46, 0x2ea10000
	s_mov_b32 s47, 0x600000
	s_mov_b32 s48, 0x610000
	s_mov_b32 s49, 0x620000
	s_mov_b32 s50, 0x6c0000
	s_mov_b32 s51, 0x6d0000
	s_mov_b32 s52, 0x6e0000
	v_mov_b32_e32 v188, 0x358637bd
	s_mov_b32 s53, 0xf800000
	v_mov_b32_e32 v189, 0x260
	v_add_u32_e32 v190, v6, v7
	s_mov_b32 s54, 0xff61b1e6
	v_mov_b32_e32 v191, 1
	v_mov_b32_e32 v192, 0xff61b1e6
	v_lshlrev_b64 v[108:109], 2, v[60:61]
	v_lshlrev_b64 v[110:111], 2, v[0:1]
	v_lshlrev_b64 v[112:113], 2, v[2:3]
	s_mov_b32 s55, s83
	v_readlane_b32 s56, v249, 18
	v_readlane_b32 s57, v249, 19
	v_readlane_b32 s58, v249, 20
	v_readlane_b32 s59, v249, 21
	s_branch .LBB0_975

; __device__ __forceinline__ void phase_router(const Args& a, unsigned char* lds_g, int tid, int lane, int wave) {
;     ...
;     for (int tp = blockIdx.x; tp < NLAT / 32; tp += gridDim.x) {
;         const int tok0 = 32 * tp + 16 * slot, b = tok0 >> 11, kbase = wave * 256 + 8 * gq;
;         const bf16* xr0 = X1 + (size_t)(32 * tp + i) * D + kbase; const bf16* xr1 = xr0 + (size_t)16 * D;
;         const bf16* wh = WRh + ((size_t)(b * 48 + i) * 2048 + kbase); const bf16* wl = WRl + ((size_t)(b * 48 + i) * 2048 + kbase);
;         f32x4 ac[2][3]; float sq0 = 0.f, sq1 = 0.f;
; #pragma unroll
;         for (int s = 0; s < 2; ++s)
; #pragma unroll
;             for (int cb = 0; cb < 3; ++cb) ac[s][cb] = (f32x4){0.f, 0.f, 0.f, 0.f};
; #pragma unroll 4
;         for (int s8 = 0; s8 < 8; ++s8) {
;             const v4u xb0 = *(const v4u*)(xr0 + 32 * s8), xb1 = *(const v4u*)(xr1 + 32 * s8);
;             const bf16x8_t h0 = *(const bf16x8_t*)(wh + 32 * s8), h1 = *(const bf16x8_t*)(wh + 16 * 2048 + 32 * s8), h2 = *(const bf16x8_t*)(wh + 32 * 2048 + 32 * s8);
;             const bf16x8_t l0 = *(const bf16x8_t*)(wl + 32 * s8), l1 = *(const bf16x8_t*)(wl + 16 * 2048 + 32 * s8), l2 = *(const bf16x8_t*)(wl + 32 * 2048 + 32 * s8);
;             const bf16x8_t xf0 = __builtin_bit_cast(bf16x8_t, xb0), xf1 = __builtin_bit_cast(bf16x8_t, xb1);
;             ac[0][0] = __builtin_amdgcn_mfma_f32_16x16x32_bf16(xf0, h0, ac[0][0], 0, 0, 0); ac[0][1] = __builtin_amdgcn_mfma_f32_16x16x32_bf16(xf0, h1, ac[0][1], 0, 0, 0); ac[0][2] = __builtin_amdgcn_mfma_f32_16x16x32_bf16(xf0, h2, ac[0][2], 0, 0, 0);
;             ac[1][0] = __builtin_amdgcn_mfma_f32_16x16x32_bf16(xf1, h0, ac[1][0], 0, 0, 0); ac[1][1] = __builtin_amdgcn_mfma_f32_16x16x32_bf16(xf1, h1, ac[1][1], 0, 0, 0); ac[1][2] = __builtin_amdgcn_mfma_f32_16x16x32_bf16(xf1, h2, ac[1][2], 0, 0, 0);
;             ac[0][0] = __builtin_amdgcn_mfma_f32_16x16x32_bf16(xf0, l0, ac[0][0], 0, 0, 0); ac[0][1] = __builtin_amdgcn_mfma_f32_16x16x32_bf16(xf0, l1, ac[0][1], 0, 0, 0); ac[0][2] = __builtin_amdgcn_mfma_f32_16x16x32_bf16(xf0, l2, ac[0][2], 0, 0, 0);
;             ac[1][0] = __builtin_amdgcn_mfma_f32_16x16x32_bf16(xf1, l0, ac[1][0], 0, 0, 0); ac[1][1] = __builtin_amdgcn_mfma_f32_16x16x32_bf16(xf1, l1, ac[1][1], 0, 0, 0); ac[1][2] = __builtin_amdgcn_mfma_f32_16x16x32_bf16(xf1, l2, ac[1][2], 0, 0, 0);
.LBB0_975:
	s_lshl_b32 s31, s55, 5
	s_add_i32 s56, s31, s36
	s_ashr_i32 s30, s56, 11
	s_mul_i32 s4, s30, 48
	v_ashrrev_i32_e32 v107, 31, v106
	s_waitcnt vmcnt(0)
	v_or_b32_e32 v24, s4, v174
	v_lshlrev_b64 v[0:1], 12, v[106:107]
	v_ashrrev_i32_e32 v25, 31, v24
	v_lshl_add_u64 v[26:27], v[104:105], 0, v[0:1]
	v_lshlrev_b64 v[0:1], 12, v[24:25]
	s_mul_i32 s4, s30, 0x30000
	s_add_i32 s4, s4, s100
	v_lshl_add_u32 v0, v62, 2, s4
	v_mov_b32_e32 v1, 0
	v_lshl_add_u64 v[28:29], v[0:1], 0, s[84:85]
	s_mov_b64 s[4:5], 0
	v_mov_b32_e32 v0, 0
	v_mov_b32_e32 v1, v61
	v_mov_b32_e32 v2, v61
	v_mov_b32_e32 v3, v61
	v_mov_b32_e32 v4, 0
	v_mov_b32_e32 v5, v61
	v_mov_b32_e32 v6, v61
	v_mov_b32_e32 v7, v61
	v_mov_b32_e32 v8, 0
	v_mov_b32_e32 v9, v61
	v_mov_b32_e32 v10, v61
	v_mov_b32_e32 v11, v61
	v_mov_b32_e32 v12, 0
	v_mov_b32_e32 v13, v61
	v_mov_b32_e32 v14, v61
	v_mov_b32_e32 v15, v61
	v_mov_b32_e32 v16, 0
	v_mov_b32_e32 v17, v61
	v_mov_b32_e32 v18, v61
	v_mov_b32_e32 v19, v61
	v_mov_b32_e32 v20, 0
	v_mov_b32_e32 v21, v61
	v_mov_b32_e32 v22, v61
	v_mov_b32_e32 v23, v61
	v_mov_b32_e32 v30, 0
	v_mov_b32_e32 v31, v61
.LBB0_976:
	v_lshl_add_u64 v[34:35], v[26:27], 0, s[4:5]
	v_add_co_u32_e32 v162, vcc, s45, v34
	v_lshl_add_u64 v[32:33], s[4:5], 4, v[28:29]
	s_nop 0
	v_addc_co_u32_e32 v163, vcc, 0, v35, vcc
	v_add_co_u32_e32 v158, vcc, s46, v34
	s_add_u32 s4, s4, 0x100
	s_nop 0
	v_addc_co_u32_e32 v159, vcc, 0, v35, vcc
	v_add_co_u32_e32 v194, vcc, s47, v32
	s_addc_u32 s5, s5, 0
	s_nop 0
	v_addc_co_u32_e32 v195, vcc, 0, v33, vcc
	v_add_co_u32_e32 v198, vcc, s48, v32
	s_cmpk_eq_i32 s4, 0x200
	s_nop 0
	v_addc_co_u32_e32 v199, vcc, 0, v33, vcc
	v_add_co_u32_e32 v202, vcc, s49, v32
	s_nop 1
	v_addc_co_u32_e32 v203, vcc, 0, v33, vcc
	v_add_co_u32_e32 v206, vcc, s50, v32
	s_nop 1
	v_addc_co_u32_e32 v207, vcc, 0, v33, vcc
	v_add_co_u32_e32 v210, vcc, s51, v32
	s_nop 1
	v_addc_co_u32_e32 v211, vcc, 0, v33, vcc
	v_add_co_u32_e32 v214, vcc, s52, v32
	s_nop 1
	v_addc_co_u32_e32 v215, vcc, 0, v33, vcc
	global_load_dwordx4 v[32:35], v[162:163], off
	global_load_dwordx4 v[36:39], v[194:195], off
	global_load_dwordx4 v[40:43], v[158:159], off
	global_load_dwordx4 v[44:47], v[202:203], off
	global_load_dwordx4 v[48:51], v[198:199], off
	global_load_dwordx4 v[52:55], v[206:207], off
	global_load_dwordx4 v[56:59], v[214:215], off
	global_load_dwordx4 v[114:117], v[210:211], off
	global_load_dwordx4 v[118:121], v[162:163], off offset:64
	global_load_dwordx4 v[122:125], v[194:195], off offset:1024
	global_load_dwordx4 v[126:129], v[158:159], off offset:64
	global_load_dwordx4 v[130:133], v[202:203], off offset:1024
	global_load_dwordx4 v[134:137], v[198:199], off offset:1024
	global_load_dwordx4 v[138:141], v[206:207], off offset:1024
	global_load_dwordx4 v[142:145], v[214:215], off offset:1024
	global_load_dwordx4 v[146:149], v[210:211], off offset:1024
	global_load_dwordx4 v[150:153], v[158:159], off offset:128
	s_waitcnt vmcnt(15)
	v_mfma_f32_16x16x32_bf16 v[0:3], v[32:35], v[36:39], v[0:3]
	s_waitcnt vmcnt(14)
	v_and_b32_e32 v217, 0xffff0000, v42
	v_and_b32_e32 v216, 0xffff0000, v34
	v_lshlrev_b32_e32 v219, 16, v43
	s_waitcnt vmcnt(12)
	v_mfma_f32_16x16x32_bf16 v[16:19], v[40:43], v[48:51], v[16:19]
	v_mul_f32_e64 v216, v216, v216
	v_mul_f32_e64 v217, v217, v217
	v_lshlrev_b32_e32 v218, 16, v35
	s_waitcnt vmcnt(8)
	v_and_b32_e32 v220, 0xffff0000, v121
	v_mfma_f32_16x16x32_bf16 v[4:7], v[32:35], v[48:51], v[4:7]
	global_load_dwordx4 v[48:51], v[162:163], off offset:128
	s_waitcnt vmcnt(7)
	v_and_b32_e32 v221, 0xffff0000, v129
	v_mfma_f32_16x16x32_bf16 v[8:11], v[32:35], v[44:47], v[8:11]
	v_mfma_f32_16x16x32_bf16 v[12:15], v[40:43], v[36:39], v[12:15]
	global_load_dwordx4 v[36:39], v[194:195], off offset:2048
	v_mfma_f32_16x16x32_bf16 v[20:23], v[40:43], v[44:47], v[20:23]
	global_load_dwordx4 v[44:47], v[202:203], off offset:2048
	global_load_dwordx4 v[154:157], v[198:199], off offset:2048
	s_nop 0
	global_load_dwordx4 v[158:161], v[158:159], off offset:192
	s_nop 0
	global_load_dwordx4 v[162:165], v[162:163], off offset:192
	s_nop 0
	global_load_dwordx4 v[166:169], v[206:207], off offset:2048
	global_load_dwordx4 v[170:173], v[214:215], off offset:2048
	v_mfma_f32_16x16x32_bf16 v[16:19], v[40:43], v[114:117], v[16:19]
	global_load_dwordx4 v[194:197], v[194:195], off offset:3072
	s_nop 0
	global_load_dwordx4 v[198:201], v[198:199], off offset:3072
	s_nop 0
	global_load_dwordx4 v[202:205], v[202:203], off offset:3072
	v_mfma_f32_16x16x32_bf16 v[4:7], v[32:35], v[114:117], v[4:7]
	global_load_dwordx4 v[114:117], v[206:207], off offset:3072
	s_nop 0
	global_load_dwordx4 v[206:209], v[210:211], off offset:2048
	s_nop 0
	global_load_dwordx4 v[210:213], v[210:211], off offset:3072
	v_mfma_f32_16x16x32_bf16 v[0:3], v[32:35], v[52:55], v[0:3]
	v_mfma_f32_16x16x32_bf16 v[12:15], v[40:43], v[52:55], v[12:15]
	global_load_dwordx4 v[52:55], v[214:215], off offset:3072
	v_lshlrev_b32_e32 v215, 16, v40
	v_lshlrev_b32_e32 v214, 16, v32
	v_mfma_f32_16x16x32_bf16 v[8:11], v[32:35], v[56:59], v[8:11]
	v_mfma_f32_16x16x32_bf16 v[20:23], v[40:43], v[56:59], v[20:23]
	v_and_b32_e32 v57, 0xffff0000, v40
	v_and_b32_e32 v56, 0xffff0000, v32
	v_lshlrev_b32_e32 v59, 16, v41
	v_mfma_f32_16x16x32_bf16 v[0:3], v[118:121], v[122:125], v[0:3]
	v_and_b32_e32 v41, 0xffff0000, v41
	v_and_b32_e32 v40, 0xffff0000, v33
	v_pk_mul_f32 v[56:57], v[56:57], v[56:57]
	s_waitcnt vmcnt(20)
	v_mfma_f32_16x16x32_bf16 v[8:11], v[118:121], v[130:133], v[8:11]
	v_lshlrev_b32_e32 v58, 16, v33
	v_pk_mul_f32 v[40:41], v[40:41], v[40:41]
	v_pk_fma_f32 v[56:57], v[214:215], v[214:215], v[56:57]
	s_waitcnt vmcnt(19)
; __device__ __forceinline__ void phase_router(const Args& a, unsigned char* lds_g, int tid, int lane, int wave) {
;     ...
;         for (int s8 = 0; s8 < 8; ++s8) {
;             const v4u xb0 = *(const v4u*)(xr0 + 32 * s8), xb1 = *(const v4u*)(xr1 + 32 * s8);
;             const bf16x8_t h0 = *(const bf16x8_t*)(wh + 32 * s8), h1 = *(const bf16x8_t*)(wh + 16 * 2048 + 32 * s8), h2 = *(const bf16x8_t*)(wh + 32 * 2048 + 32 * s8);
;             const bf16x8_t l0 = *(const bf16x8_t*)(wl + 32 * s8), l1 = *(const bf16x8_t*)(wl + 16 * 2048 + 32 * s8), l2 = *(const bf16x8_t*)(wl + 32 * 2048 + 32 * s8);
;             const bf16x8_t xf0 = __builtin_bit_cast(bf16x8_t, xb0), xf1 = __builtin_bit_cast(bf16x8_t, xb1);
;             ac[0][0] = __builtin_amdgcn_mfma_f32_16x16x32_bf16(xf0, h0, ac[0][0], 0, 0, 0); ac[0][1] = __builtin_amdgcn_mfma_f32_16x16x32_bf16(xf0, h1, ac[0][1], 0, 0, 0); ac[0][2] = __builtin_amdgcn_mfma_f32_16x16x32_bf16(xf0, h2, ac[0][2], 0, 0, 0);
;             ac[1][0] = __builtin_amdgcn_mfma_f32_16x16x32_bf16(xf1, h0, ac[1][0], 0, 0, 0); ac[1][1] = __builtin_amdgcn_mfma_f32_16x16x32_bf16(xf1, h1, ac[1][1], 0, 0, 0); ac[1][2] = __builtin_amdgcn_mfma_f32_16x16x32_bf16(xf1, h2, ac[1][2], 0, 0, 0);
;             ac[0][0] = __builtin_amdgcn_mfma_f32_16x16x32_bf16(xf0, l0, ac[0][0], 0, 0, 0); ac[0][1] = __builtin_amdgcn_mfma_f32_16x16x32_bf16(xf0, l1, ac[0][1], 0, 0, 0); ac[0][2] = __builtin_amdgcn_mfma_f32_16x16x32_bf16(xf0, l2, ac[0][2], 0, 0, 0);
;             ac[1][0] = __builtin_amdgcn_mfma_f32_16x16x32_bf16(xf1, l0, ac[1][0], 0, 0, 0); ac[1][1] = __builtin_amdgcn_mfma_f32_16x16x32_bf16(xf1, l1, ac[1][1], 0, 0, 0); ac[1][2] = __builtin_amdgcn_mfma_f32_16x16x32_bf16(xf1, l2, ac[1][2], 0, 0, 0);
;             const unsigned xw0[4] = {xb0.x, xb0.y, xb0.z, xb0.w}, xw1[4] = {xb1.x, xb1.y, xb1.z, xb1.w};
; #pragma unroll
;             for (int e = 0; e < 4; ++e) { sq0 += bflo(xw0[e]) * bflo(xw0[e]) + bfhi(xw0[e]) * bfhi(xw0[e]); sq1 += bflo(xw1[e]) * bflo(xw1[e]) + bfhi(xw1[e]) * bfhi(xw1[e]); }
;         }
	v_mfma_f32_16x16x32_bf16 v[4:7], v[118:121], v[134:137], v[4:7]
	v_lshlrev_b32_e32 v33, 16, v42
	v_lshlrev_b32_e32 v32, 16, v34
	v_and_b32_e32 v43, 0xffff0000, v43
	v_mfma_f32_16x16x32_bf16 v[16:19], v[126:129], v[134:137], v[16:19]
	v_and_b32_e32 v42, 0xffff0000, v35
	v_pk_fma_f32 v[40:41], v[58:59], v[58:59], v[40:41]
	v_pk_add_f32 v[30:31], v[30:31], v[56:57]
	v_mfma_f32_16x16x32_bf16 v[12:15], v[126:129], v[122:125], v[12:15]
	v_and_b32_e32 v123, 0xffff0000, v126
	v_and_b32_e32 v122, 0xffff0000, v118
	v_pk_mul_f32 v[42:43], v[42:43], v[42:43]
	v_mfma_f32_16x16x32_bf16 v[20:23], v[126:129], v[130:133], v[20:23]
	v_fma_f32 v32, v32, v32, v216
	v_fma_f32 v33, v33, v33, v217
	v_pk_add_f32 v[30:31], v[40:41], v[30:31]
	v_lshlrev_b32_e32 v35, 16, v126
	s_waitcnt vmcnt(18)
	v_mfma_f32_16x16x32_bf16 v[0:3], v[118:121], v[138:141], v[0:3]
	v_lshlrev_b32_e32 v34, 16, v118
	v_and_b32_e32 v131, 0xffff0000, v127
	v_and_b32_e32 v130, 0xffff0000, v119
	s_waitcnt vmcnt(17)
	v_mfma_f32_16x16x32_bf16 v[8:11], v[118:121], v[142:145], v[8:11]
	v_lshlrev_b32_e32 v132, 16, v120
	v_and_b32_e32 v134, 0xffff0000, v120
	v_pk_fma_f32 v[42:43], v[218:219], v[218:219], v[42:43]
	s_waitcnt vmcnt(16)
	v_mfma_f32_16x16x32_bf16 v[4:7], v[118:121], v[146:149], v[4:7]
	v_add_f32_e64 v30, v32, v30
	v_add_f32_e64 v31, v33, v31
	v_lshlrev_b32_e32 v125, 16, v127
	v_lshlrev_b32_e32 v124, 16, v119
	v_mfma_f32_16x16x32_bf16 v[16:19], v[126:129], v[146:149], v[16:19]
	v_lshlrev_b32_e32 v133, 16, v128
	v_and_b32_e32 v135, 0xffff0000, v128
	v_pk_add_f32 v[30:31], v[42:43], v[30:31]
	v_mfma_f32_16x16x32_bf16 v[12:15], v[126:129], v[138:141], v[12:15]
	s_waitcnt vmcnt(14)
	v_lshlrev_b32_e32 v118, 16, v48
	v_and_b32_e32 v120, 0xffff0000, v48
	v_lshlrev_b32_e32 v138, 16, v49
	v_mfma_f32_16x16x32_bf16 v[20:23], v[126:129], v[142:145], v[20:23]
	v_and_b32_e32 v126, 0xffff0000, v49
	v_lshlrev_b32_e32 v128, 16, v50
	v_and_b32_e32 v140, 0xffff0000, v50
	s_waitcnt vmcnt(13)
	v_mfma_f32_16x16x32_bf16 v[0:3], v[48:51], v[36:39], v[0:3]
	v_lshlrev_b32_e32 v142, 16, v51
	v_and_b32_e32 v144, 0xffff0000, v51
	v_lshlrev_b32_e32 v137, 16, v129
	s_waitcnt vmcnt(12)
	v_mfma_f32_16x16x32_bf16 v[8:11], v[48:51], v[44:47], v[8:11]
	v_lshlrev_b32_e32 v136, 16, v121
	v_and_b32_e32 v121, 0xffff0000, v150
	v_lshlrev_b32_e32 v119, 16, v150
	s_waitcnt vmcnt(11)
	v_mfma_f32_16x16x32_bf16 v[4:7], v[48:51], v[154:157], v[4:7]
	v_and_b32_e32 v127, 0xffff0000, v151
	v_pk_mul_f32 v[120:121], v[120:121], v[120:121]
	v_lshlrev_b32_e32 v139, 16, v151
	v_mfma_f32_16x16x32_bf16 v[16:19], v[150:153], v[154:157], v[16:19]
	v_and_b32_e32 v141, 0xffff0000, v152
	v_pk_mul_f32 v[126:127], v[126:127], v[126:127]
	v_pk_fma_f32 v[118:119], v[118:119], v[118:119], v[120:121]
	v_mfma_f32_16x16x32_bf16 v[12:15], v[150:153], v[36:39], v[12:15]
	v_lshlrev_b32_e32 v129, 16, v152
	v_and_b32_e32 v145, 0xffff0000, v153
	v_pk_fma_f32 v[120:121], v[138:139], v[138:139], v[126:127]
	v_mfma_f32_16x16x32_bf16 v[20:23], v[150:153], v[44:47], v[20:23]
	v_lshlrev_b32_e32 v143, 16, v153
	s_waitcnt vmcnt(10)
	v_and_b32_e32 v149, 0xffff0000, v158
	s_waitcnt vmcnt(9)
	v_and_b32_e32 v148, 0xffff0000, v162
	s_waitcnt vmcnt(8)
	v_mfma_f32_16x16x32_bf16 v[0:3], v[48:51], v[166:169], v[0:3]
	v_lshlrev_b32_e32 v147, 16, v158
	v_lshlrev_b32_e32 v146, 16, v162
	v_and_b32_e32 v39, 0xffff0000, v159
	s_waitcnt vmcnt(7)
	v_mfma_f32_16x16x32_bf16 v[8:11], v[48:51], v[170:173], v[8:11]
	v_and_b32_e32 v38, 0xffff0000, v163
	v_lshlrev_b32_e32 v37, 16, v159
	v_lshlrev_b32_e32 v36, 16, v163
	s_waitcnt vmcnt(2)
	v_mfma_f32_16x16x32_bf16 v[4:7], v[48:51], v[206:209], v[4:7]
	v_mul_f32_e64 v48, v122, v122
	v_mul_f32_e64 v49, v123, v123
	v_pk_mul_f32 v[50:51], v[130:131], v[130:131]
	v_pk_fma_f32 v[34:35], v[34:35], v[34:35], v[48:49]
	v_mfma_f32_16x16x32_bf16 v[16:19], v[150:153], v[206:209], v[16:19]
	v_mul_f32_e64 v122, v134, v134
	v_mul_f32_e64 v123, v135, v135
	v_pk_fma_f32 v[48:49], v[124:125], v[124:125], v[50:51]
	v_pk_add_f32 v[30:31], v[30:31], v[34:35]
	v_mfma_f32_16x16x32_bf16 v[12:15], v[150:153], v[166:169], v[12:15]
	v_mul_f32_e64 v130, v220, v220
	v_mul_f32_e64 v131, v221, v221
	v_pk_fma_f32 v[50:51], v[132:133], v[132:133], v[122:123]
	v_pk_add_f32 v[30:31], v[48:49], v[30:31]
	v_mfma_f32_16x16x32_bf16 v[20:23], v[150:153], v[170:173], v[20:23]
	v_fma_f32 v58, v136, v136, v130
	v_fma_f32 v59, v137, v137, v131
	v_pk_add_f32 v[30:31], v[50:51], v[30:31]
	v_pk_mul_f32 v[134:135], v[140:141], v[140:141]
	v_pk_add_f32 v[30:31], v[58:59], v[30:31]
	v_mfma_f32_16x16x32_bf16 v[0:3], v[162:165], v[194:197], v[0:3]
	v_add_f32_e64 v30, v30, v118
	v_add_f32_e64 v31, v31, v119
	v_pk_mul_f32 v[140:141], v[144:145], v[144:145]
	v_pk_fma_f32 v[122:123], v[128:129], v[128:129], v[134:135]
	v_mfma_f32_16x16x32_bf16 v[8:11], v[162:165], v[202:205], v[8:11]
	v_add_f32_e64 v30, v120, v30
	v_add_f32_e64 v31, v121, v31
	v_pk_mul_f32 v[144:145], v[148:149], v[148:149]
	v_pk_fma_f32 v[124:125], v[142:143], v[142:143], v[140:141]
	v_mfma_f32_16x16x32_bf16 v[16:19], v[158:161], v[198:201], v[16:19]
	v_add_f32_e64 v30, v122, v30
	v_add_f32_e64 v31, v123, v31
	v_and_b32_e32 v47, 0xffff0000, v160
	v_and_b32_e32 v46, 0xffff0000, v164
	v_mfma_f32_16x16x32_bf16 v[4:7], v[162:165], v[198:201], v[4:7]
	v_mul_f32_e64 v38, v38, v38
	v_mul_f32_e64 v39, v39, v39
	v_pk_fma_f32 v[126:127], v[146:147], v[146:147], v[144:145]
	v_pk_add_f32 v[30:31], v[124:125], v[30:31]
	v_mfma_f32_16x16x32_bf16 v[12:15], v[158:161], v[194:197], v[12:15]
	v_lshlrev_b32_e32 v45, 16, v160
	v_lshlrev_b32_e32 v44, 16, v164
	v_and_b32_e32 v157, 0xffff0000, v161
	v_mfma_f32_16x16x32_bf16 v[20:23], v[158:161], v[202:205], v[20:23]
	v_and_b32_e32 v156, 0xffff0000, v165
	v_pk_mul_f32 v[46:47], v[46:47], v[46:47]
	v_pk_fma_f32 v[36:37], v[36:37], v[36:37], v[38:39]
	v_mfma_f32_16x16x32_bf16 v[0:3], v[162:165], v[114:117], v[0:3]
	v_add_f32_e64 v30, v30, v126
	v_add_f32_e64 v31, v31, v127
	v_lshlrev_b32_e32 v155, 16, v161
	v_lshlrev_b32_e32 v154, 16, v165
	s_waitcnt vmcnt(0)
	v_mfma_f32_16x16x32_bf16 v[8:11], v[162:165], v[52:55], v[8:11]
	v_mul_f32_e64 v148, v156, v156
	v_mul_f32_e64 v149, v157, v157
	v_pk_fma_f32 v[38:39], v[44:45], v[44:45], v[46:47]
	v_pk_add_f32 v[30:31], v[36:37], v[30:31]
	v_mfma_f32_16x16x32_bf16 v[16:19], v[158:161], v[210:213], v[16:19]
	v_fma_f32 v44, v154, v154, v148
	v_fma_f32 v45, v155, v155, v149
	v_pk_add_f32 v[30:31], v[38:39], v[30:31]
	v_mfma_f32_16x16x32_bf16 v[4:7], v[162:165], v[210:213], v[4:7]
	v_add_f32_e64 v30, v44, v30
	v_add_f32_e64 v31, v45, v31
	v_mfma_f32_16x16x32_bf16 v[12:15], v[158:161], v[114:117], v[12:15]
	v_mfma_f32_16x16x32_bf16 v[20:23], v[158:161], v[52:55], v[20:23]
	s_cbranch_scc0 .LBB0_976
; __device__ __forceinline__ void phase_router(const Args& a, unsigned char* lds_g, int tid, int lane, int wave) {
;     ...
;         sq0 += __shfl_xor(sq0, 16); sq0 += __shfl_xor(sq0, 32); sq1 += __shfl_xor(sq1, 16); sq1 += __shfl_xor(sq1, 32);
; #pragma unroll
;         for (int s = 0; s < 2; ++s)
; #pragma unroll
;             for (int cb = 0; cb < 3; ++cb) PART[((s * 8 + wave) * 3 + cb) * 64 + lane] = ac[s][cb];
;         if (gq == 0) { SSQP[(0 * 8 + wave) * 16 + i] = sq0; SSQP[(1 * 8 + wave) * 16 + i] = sq1; }
;         __syncthreads();
;         if (wave < 2) { const int slot = wave; const int tok0 = 32 * tp + 16 * slot;
;             const float* sp = SSQP + slot * 128; const float rstd = 1.f / sqrtf((((sp[i] + sp[16 + i]) + (sp[32 + i] + sp[48 + i])) + ((sp[64 + i] + sp[80 + i]) + (sp[96 + i] + sp[112 + i]))) * (1.f / D) + EPS);
;             if (gq == 0) RS[slot * 16 + i] = rstd;
	ds_bpermute_b32 v26, v175, v30
	ds_bpermute_b32 v27, v175, v31
	v_add_u32_e32 v32, s38, v64
	ds_write_b128 v32, v[0:3]
	ds_write_b128 v32, v[4:7] offset:1024
	ds_write_b128 v32, v[8:11] offset:2048
	ds_write_b128 v32, v[12:15] offset:24576
	ds_write_b128 v32, v[16:19] offset:25600
	ds_write_b128 v32, v[20:23] offset:26624
	s_waitcnt lgkmcnt(0)
	v_add_f32_e32 v26, v30, v26
	v_add_f32_e32 v27, v31, v27
	ds_bpermute_b32 v28, v176, v26
	ds_bpermute_b32 v29, v176, v27
	s_and_saveexec_b64 s[4:5], s[0:1]
	s_cbranch_execz .LBB0_979
	s_waitcnt lgkmcnt(1)
	v_add_f32_e32 v0, v26, v28
	s_waitcnt lgkmcnt(0)
	v_add_f32_e32 v1, v27, v29
	ds_write_b32 v65, v0 offset:49152
	ds_write_b32 v177, v1 offset:49664
